# one static s_setprio 1 for waves 0-3 at kernel entry
# speedup vs baseline: 1.0010x; 1.0010x over previous
.LBB0_7:
	s_or_b64 exec, exec, s[4:5]
	s_lshr_b32 s65, s3, 6
	s_cmp_gt_u32 s65, 3
	s_cbranch_scc1 .Lprio_done
	s_setprio 1
